# COUT epilogue: touch second-half residual lines early (extra dword loads) so the later half-1 loads hit cache
# baseline (speedup 1.0000x reference)
; #define EPIRES_LOAD(ai) do { _Pragma("unroll") for (int m = 0; m < 4; ++m) { const size_t off = (size_t)(row0 + (ai) * HALF + m * 16) * ldc + col0; \
;             _Pragma("unroll") for (int bj = 0; bj < 2; ++bj) bw[m][bj] = *(const u32x4*)((const bf16_t*)base + off + bj * HALF); } asm volatile("" ::: "memory"); } while (0)
;     __device__ __forceinline__ void operator()(const f32x4 (&acc)[2][2][4][2], const Unit& u, int wr, int wc, int fr, int fq, const Pre&) const {
;         const int row0 = u.pm * BM + wr * 64 + fr, col0 = u.pn * BM + wc * 32 + 8 * fq;
;         static_assert(BASE_BF16, "only the bf16 residual base is in use");
;         u32x4 bw[4][2], pk[4][2];
;     ...
;         EPIRES_LOAD(0);
; #pragma unroll
;         for (int m = 0; m < 4; ++m)
; #pragma unroll
;             for (int bj = 0; bj < 2; ++bj) pk[m][bj] = EPIRES_CALC(0, m, bj);
.LBB0_1201:
	s_mov_b64 s[98:99], 0x80000
	v_lshl_or_b32 v132, s73, 8, v167
	v_lshl_add_u32 v130, s50, 8, v1
	v_ashrrev_i32_e32 v133, 31, v132
	v_lshlrev_b64 v[154:155], 1, v[132:133]
	v_ashrrev_i32_e32 v131, 31, v130
	v_lshl_add_u64 v[156:157], s[12:13], 0, v[154:155]
	v_lshlrev_b64 v[158:159], 12, v[130:131]
	v_lshl_add_u64 v[132:133], v[156:157], 0, v[158:159]
	v_lshl_add_u64 v[246:247], v[132:133], 0, s[98:99]
	global_load_dword v248, v[246:247], off
	global_load_dwordx4 v[172:175], v[132:133], off
	v_lshl_add_u64 v[244:245], v[132:133], 0, s[98:99]
	global_load_dword v249, v[244:245], off offset:256
	global_load_dwordx4 v[176:179], v[132:133], off offset:256
	v_or_b32_e32 v132, 16, v130
	v_ashrrev_i32_e32 v133, 31, v132
	v_lshlrev_b64 v[160:161], 12, v[132:133]
	v_lshl_add_u64 v[132:133], v[156:157], 0, v[160:161]
	v_lshl_add_u64 v[246:247], v[132:133], 0, s[98:99]
	global_load_dword v250, v[246:247], off
	global_load_dwordx4 v[180:183], v[132:133], off
	v_lshl_add_u64 v[244:245], v[132:133], 0, s[98:99]
	global_load_dword v251, v[244:245], off offset:256
	global_load_dwordx4 v[184:187], v[132:133], off offset:256
	v_or_b32_e32 v132, 32, v130
	v_ashrrev_i32_e32 v133, 31, v132
	v_lshlrev_b64 v[162:163], 12, v[132:133]
	v_lshl_add_u64 v[132:133], v[156:157], 0, v[162:163]
	v_lshl_add_u64 v[246:247], v[132:133], 0, s[98:99]
	global_load_dword v252, v[246:247], off
	global_load_dwordx4 v[188:191], v[132:133], off
	v_or_b32_e32 v130, 48, v130
	v_ashrrev_i32_e32 v131, 31, v130
	v_lshlrev_b64 v[164:165], 12, v[130:131]
	v_lshl_add_u64 v[130:131], v[156:157], 0, v[164:165]
	v_lshl_add_u64 v[244:245], v[132:133], 0, s[98:99]
	global_load_dword v253, v[244:245], off offset:256
	global_load_dwordx4 v[192:195], v[132:133], off offset:256
	v_lshl_add_u64 v[246:247], v[130:131], 0, s[98:99]
	global_load_dword v254, v[246:247], off
	global_load_dwordx4 v[134:137], v[130:131], off
	s_nop 0
	v_lshl_add_u64 v[244:245], v[130:131], 0, s[98:99]
	global_load_dword v255, v[244:245], off offset:256
	global_load_dwordx4 v[130:133], v[130:131], off offset:256
	s_andn2_b64 vcc, exec, s[10:11]
	s_mov_b64 s[10:11], -1
	s_waitcnt vmcnt(0)
	v_lshlrev_b32_e32 v196, 16, v172
	v_lshlrev_b32_e32 v200, 16, v176
	v_and_b32_e32 v201, 0xffff0000, v176
	v_lshlrev_b32_e32 v176, 16, v177
	v_and_b32_e32 v177, 0xffff0000, v177
	v_lshlrev_b32_e32 v202, 16, v178
	v_and_b32_e32 v203, 0xffff0000, v178
	v_lshlrev_b32_e32 v178, 16, v179
	v_and_b32_e32 v179, 0xffff0000, v179
	v_lshlrev_b32_e32 v206, 16, v182
	v_and_b32_e32 v207, 0xffff0000, v182
	v_lshlrev_b32_e32 v182, 16, v183
	v_and_b32_e32 v183, 0xffff0000, v183
	v_lshlrev_b32_e32 v210, 16, v186
	v_and_b32_e32 v211, 0xffff0000, v186
	v_and_b32_e32 v197, 0xffff0000, v172
	v_lshlrev_b32_e32 v172, 16, v173
	v_and_b32_e32 v173, 0xffff0000, v173
	v_lshlrev_b32_e32 v198, 16, v174
	v_and_b32_e32 v199, 0xffff0000, v174
	v_lshlrev_b32_e32 v174, 16, v175
	v_and_b32_e32 v175, 0xffff0000, v175
	v_lshlrev_b32_e32 v204, 16, v180
	v_and_b32_e32 v205, 0xffff0000, v180
	v_lshlrev_b32_e32 v180, 16, v181
	v_and_b32_e32 v181, 0xffff0000, v181
	v_lshlrev_b32_e32 v208, 16, v184
	v_and_b32_e32 v209, 0xffff0000, v184
	v_lshlrev_b32_e32 v184, 16, v185
	v_and_b32_e32 v185, 0xffff0000, v185
	v_lshlrev_b32_e32 v186, 16, v187
	v_and_b32_e32 v187, 0xffff0000, v187
	v_pk_add_f32 v[112:113], v[112:113], v[176:177]
	v_pk_add_f32 v[110:111], v[110:111], v[200:201]
	v_pk_add_f32 v[108:109], v[108:109], v[178:179]
	v_pk_add_f32 v[106:107], v[106:107], v[202:203]
	v_pk_add_f32 v[116:117], v[116:117], v[182:183]
	v_pk_add_f32 v[114:115], v[114:115], v[206:207]
	v_pk_add_f32 v[98:99], v[98:99], v[210:211]
	v_pk_add_f32 v[128:129], v[128:129], v[172:173]
	v_pk_add_f32 v[126:127], v[126:127], v[196:197]
	v_pk_add_f32 v[124:125], v[124:125], v[174:175]
	v_pk_add_f32 v[122:123], v[122:123], v[198:199]
	v_pk_add_f32 v[120:121], v[120:121], v[180:181]
	v_pk_add_f32 v[118:119], v[118:119], v[204:205]
	v_pk_add_f32 v[172:173], v[104:105], v[184:185]
	v_pk_add_f32 v[174:175], v[102:103], v[208:209]
	v_pk_add_f32 v[176:177], v[100:101], v[186:187]
	v_cvt_pk_bf16_f32 v100, v126, v127
	v_cvt_pk_bf16_f32 v101, v128, v129
	v_cvt_pk_bf16_f32 v102, v122, v123
	v_cvt_pk_bf16_f32 v103, v124, v125
	v_cvt_pk_bf16_f32 v104, v110, v111
	v_cvt_pk_bf16_f32 v105, v112, v113
	v_cvt_pk_bf16_f32 v106, v106, v107
	v_cvt_pk_bf16_f32 v107, v108, v109
	v_cvt_pk_bf16_f32 v108, v118, v119
	v_cvt_pk_bf16_f32 v109, v120, v121
	v_cvt_pk_bf16_f32 v110, v114, v115
	v_cvt_pk_bf16_f32 v111, v116, v117
	v_cvt_pk_bf16_f32 v112, v174, v175
	v_cvt_pk_bf16_f32 v113, v172, v173
	v_cvt_pk_bf16_f32 v114, v98, v99
	v_lshlrev_b32_e32 v98, 16, v188
	v_and_b32_e32 v99, 0xffff0000, v188
	v_lshlrev_b32_e32 v116, 16, v189
	v_and_b32_e32 v117, 0xffff0000, v189
	v_lshlrev_b32_e32 v118, 16, v190
	v_and_b32_e32 v119, 0xffff0000, v190
	v_lshlrev_b32_e32 v120, 16, v191
	v_and_b32_e32 v121, 0xffff0000, v191
	v_pk_add_f32 v[96:97], v[96:97], v[116:117]
	v_pk_add_f32 v[94:95], v[94:95], v[98:99]
	v_cvt_pk_bf16_f32 v115, v176, v177
	v_pk_add_f32 v[98:99], v[92:93], v[120:121]
	v_pk_add_f32 v[92:93], v[90:91], v[118:119]
	v_cvt_pk_bf16_f32 v90, v94, v95
	v_cvt_pk_bf16_f32 v91, v96, v97
	v_lshlrev_b32_e32 v94, 16, v192
	v_and_b32_e32 v95, 0xffff0000, v192
	v_lshlrev_b32_e32 v96, 16, v193
	v_and_b32_e32 v97, 0xffff0000, v193
	v_cvt_pk_bf16_f32 v92, v92, v93
	v_cvt_pk_bf16_f32 v93, v98, v99
	v_lshlrev_b32_e32 v98, 16, v194
	v_and_b32_e32 v99, 0xffff0000, v194
	v_lshlrev_b32_e32 v116, 16, v195
	v_and_b32_e32 v117, 0xffff0000, v195
	v_pk_add_f32 v[88:89], v[88:89], v[96:97]
	v_pk_add_f32 v[86:87], v[86:87], v[94:95]
; #define EPIRES_LOAD(ai) do { _Pragma("unroll") for (int m = 0; m < 4; ++m) { const size_t off = (size_t)(row0 + (ai) * HALF + m * 16) * ldc + col0; \
;             _Pragma("unroll") for (int bj = 0; bj < 2; ++bj) bw[m][bj] = *(const u32x4*)((const bf16_t*)base + off + bj * HALF); } asm volatile("" ::: "memory"); } while (0)
;     __device__ __forceinline__ void operator()(const f32x4 (&acc)[2][2][4][2], const Unit& u, int wr, int wc, int fr, int fq, const Pre&) const {
;     ...
;         EPIRES_LOAD(1);
; #pragma unroll
;         for (int m = 0; m < 4; ++m) { const size_t off = (size_t)(row0 + m * 16) * ldc + col0;
; #pragma unroll
;             for (int bj = 0; bj < 2; ++bj) *(u32x4*)(out + off + bj * HALF) = pk[m][bj]; }
;         asm volatile("" ::: "memory");
; #pragma unroll
;         for (int m = 0; m < 4; ++m) { const size_t off = (size_t)(row0 + HALF + m * 16) * ldc + col0;
; #pragma unroll
;             for (int bj = 0; bj < 2; ++bj) *(u32x4*)(out + off + bj * HALF) = EPIRES_CALC(1, m, bj); }
	v_pk_add_f32 v[94:95], v[84:85], v[116:117]
	v_pk_add_f32 v[84:85], v[82:83], v[98:99]
	v_cvt_pk_bf16_f32 v82, v86, v87
	v_cvt_pk_bf16_f32 v83, v88, v89
	v_lshlrev_b32_e32 v86, 16, v134
	v_and_b32_e32 v87, 0xffff0000, v134
	v_lshlrev_b32_e32 v88, 16, v135
	v_and_b32_e32 v89, 0xffff0000, v135
	v_lshlrev_b32_e32 v96, 16, v137
	v_and_b32_e32 v97, 0xffff0000, v137
	v_cvt_pk_bf16_f32 v84, v84, v85
	v_cvt_pk_bf16_f32 v85, v94, v95
	v_lshlrev_b32_e32 v94, 16, v136
	v_and_b32_e32 v95, 0xffff0000, v136
	v_pk_add_f32 v[80:81], v[80:81], v[88:89]
	v_pk_add_f32 v[78:79], v[78:79], v[86:87]
	v_pk_add_f32 v[86:87], v[76:77], v[96:97]
	v_pk_add_f32 v[74:75], v[74:75], v[94:95]
	v_cvt_pk_bf16_f32 v76, v78, v79
	v_cvt_pk_bf16_f32 v77, v80, v81
	v_lshlrev_b32_e32 v80, 16, v131
	v_cvt_pk_bf16_f32 v78, v74, v75
	v_cvt_pk_bf16_f32 v79, v86, v87
	v_and_b32_e32 v81, 0xffff0000, v131
	v_lshlrev_b32_e32 v86, 16, v132
	v_and_b32_e32 v87, 0xffff0000, v132
	v_lshlrev_b32_e32 v74, 16, v130
	v_and_b32_e32 v75, 0xffff0000, v130
	v_lshlrev_b32_e32 v88, 16, v133
	v_and_b32_e32 v89, 0xffff0000, v133
	v_pk_add_f32 v[72:73], v[72:73], v[80:81]
	v_pk_add_f32 v[66:67], v[66:67], v[86:87]
	v_lshl_add_u64 v[80:81], v[158:159], 0, s[14:15]
	v_pk_add_f32 v[70:71], v[70:71], v[74:75]
	v_pk_add_f32 v[68:69], v[68:69], v[88:89]
	v_cvt_pk_bf16_f32 v86, v70, v71
	v_cvt_pk_bf16_f32 v87, v72, v73
	v_cvt_pk_bf16_f32 v88, v66, v67
	v_lshl_add_u64 v[66:67], v[156:157], 0, v[80:81]
	v_cvt_pk_bf16_f32 v89, v68, v69
	global_load_dwordx4 v[94:97], v[66:67], off
	global_load_dwordx4 v[116:119], v[66:67], off offset:256
	v_lshl_add_u64 v[98:99], v[158:159], 0, s[24:25]
	v_lshl_add_u64 v[66:67], v[156:157], 0, v[98:99]
	global_load_dwordx4 v[120:123], v[66:67], off
	global_load_dwordx4 v[124:127], v[66:67], off offset:256
	v_lshl_add_u64 v[136:137], v[158:159], 0, s[26:27]
	v_lshl_add_u64 v[66:67], v[156:157], 0, v[136:137]
	global_load_dwordx4 v[128:131], v[66:67], off
	global_load_dwordx4 v[132:135], v[66:67], off offset:256
	v_lshl_add_u64 v[74:75], v[158:159], 0, s[40:41]
	v_lshl_add_u64 v[66:67], v[156:157], 0, v[74:75]
	global_load_dwordx4 v[70:73], v[66:67], off
	s_nop 0
	global_load_dwordx4 v[66:69], v[66:67], off offset:256
	v_lshl_add_u64 v[156:157], s[20:21], 0, v[158:159]
	v_lshl_add_u64 v[156:157], v[156:157], 0, v[154:155]
	global_store_dwordx4 v[156:157], v[100:103], off
	global_store_dwordx4 v[156:157], v[104:107], off offset:256
	s_nop 0
	v_lshl_add_u64 v[100:101], s[20:21], 0, v[160:161]
	v_lshl_add_u64 v[100:101], v[100:101], 0, v[154:155]
	global_store_dwordx4 v[100:101], v[108:111], off
	global_store_dwordx4 v[100:101], v[112:115], off offset:256
	v_lshl_add_u64 v[100:101], s[20:21], 0, v[162:163]
	v_lshl_add_u64 v[100:101], v[100:101], 0, v[154:155]
	global_store_dwordx4 v[100:101], v[90:93], off
	global_store_dwordx4 v[100:101], v[82:85], off offset:256
	s_nop 1
	v_lshl_add_u64 v[82:83], s[20:21], 0, v[164:165]
	v_lshl_add_u64 v[82:83], v[82:83], 0, v[154:155]
	global_store_dwordx4 v[82:83], v[76:79], off
	global_store_dwordx4 v[82:83], v[86:89], off offset:256
	s_waitcnt vmcnt(15)
	v_lshlrev_b32_e32 v82, 16, v96
	v_lshlrev_b32_e32 v76, 16, v94
	v_and_b32_e32 v77, 0xffff0000, v94
	v_and_b32_e32 v83, 0xffff0000, v96
	v_lshlrev_b32_e32 v84, 16, v97
	v_and_b32_e32 v85, 0xffff0000, v97
	v_pk_add_f32 v[54:55], v[54:55], v[76:77]
	v_lshlrev_b32_e32 v78, 16, v95
	v_and_b32_e32 v79, 0xffff0000, v95
	v_pk_add_f32 v[76:77], v[52:53], v[84:85]
	v_pk_add_f32 v[52:53], v[50:51], v[82:83]
	v_cvt_pk_bf16_f32 v50, v54, v55
	v_lshl_add_u64 v[54:55], s[20:21], 0, v[80:81]
	v_pk_add_f32 v[56:57], v[56:57], v[78:79]
	v_lshl_add_u64 v[54:55], v[54:55], 0, v[154:155]
	v_cvt_pk_bf16_f32 v51, v56, v57
	v_cvt_pk_bf16_f32 v52, v52, v53
	v_cvt_pk_bf16_f32 v53, v76, v77
	global_store_dwordx4 v[54:55], v[50:53], off
	s_waitcnt vmcnt(15)
	v_lshlrev_b32_e32 v56, 16, v118
	v_and_b32_e32 v57, 0xffff0000, v118
	v_lshlrev_b32_e32 v50, 16, v116
	v_and_b32_e32 v51, 0xffff0000, v116
	v_lshlrev_b32_e32 v52, 16, v117
	v_and_b32_e32 v53, 0xffff0000, v117
	v_pk_add_f32 v[50:51], v[62:63], v[50:51]
	v_lshlrev_b32_e32 v76, 16, v119
	v_and_b32_e32 v77, 0xffff0000, v119
	v_pk_add_f32 v[52:53], v[64:65], v[52:53]
	v_cvt_pk_bf16_f32 v50, v50, v51
	v_pk_add_f32 v[60:61], v[60:61], v[76:77]
	v_cvt_pk_bf16_f32 v51, v52, v53
	v_pk_add_f32 v[56:57], v[58:59], v[56:57]
	s_nop 0
	v_cvt_pk_bf16_f32 v52, v56, v57
	v_cvt_pk_bf16_f32 v53, v60, v61
	global_store_dwordx4 v[54:55], v[50:53], off offset:256
	s_waitcnt vmcnt(15)
;     __device__ __forceinline__ void operator()(const f32x4 (&acc)[2][2][4][2], const Unit& u, int wr, int wc, int fr, int fq, const Pre&) const {
;     ...
;         for (int m = 0; m < 4; ++m) { const size_t off = (size_t)(row0 + HALF + m * 16) * ldc + col0;
; #pragma unroll
;             for (int bj = 0; bj < 2; ++bj) *(u32x4*)(out + off + bj * HALF) = EPIRES_CALC(1, m, bj); }
	v_lshlrev_b32_e32 v54, 16, v122
	v_and_b32_e32 v55, 0xffff0000, v122
	v_lshlrev_b32_e32 v50, 16, v120
	v_and_b32_e32 v51, 0xffff0000, v120
	v_lshlrev_b32_e32 v56, 16, v123
	v_and_b32_e32 v57, 0xffff0000, v123
	v_pk_add_f32 v[38:39], v[38:39], v[50:51]
	v_lshlrev_b32_e32 v52, 16, v121
	v_and_b32_e32 v53, 0xffff0000, v121
	v_pk_add_f32 v[50:51], v[36:37], v[56:57]
	v_pk_add_f32 v[36:37], v[34:35], v[54:55]
	v_cvt_pk_bf16_f32 v34, v38, v39
	v_lshl_add_u64 v[38:39], s[20:21], 0, v[98:99]
	v_pk_add_f32 v[40:41], v[40:41], v[52:53]
	v_lshl_add_u64 v[38:39], v[38:39], 0, v[154:155]
	v_cvt_pk_bf16_f32 v35, v40, v41
	v_cvt_pk_bf16_f32 v36, v36, v37
	v_cvt_pk_bf16_f32 v37, v50, v51
	global_store_dwordx4 v[38:39], v[34:37], off
	s_waitcnt vmcnt(15)
	v_lshlrev_b32_e32 v40, 16, v126
	v_and_b32_e32 v41, 0xffff0000, v126
	v_lshlrev_b32_e32 v34, 16, v124
	v_and_b32_e32 v35, 0xffff0000, v124
	v_lshlrev_b32_e32 v36, 16, v125
	v_and_b32_e32 v37, 0xffff0000, v125
	v_pk_add_f32 v[34:35], v[46:47], v[34:35]
	v_lshlrev_b32_e32 v50, 16, v127
	v_and_b32_e32 v51, 0xffff0000, v127
	v_pk_add_f32 v[36:37], v[48:49], v[36:37]
	v_cvt_pk_bf16_f32 v34, v34, v35
	v_pk_add_f32 v[44:45], v[44:45], v[50:51]
	v_cvt_pk_bf16_f32 v35, v36, v37
	v_pk_add_f32 v[40:41], v[42:43], v[40:41]
	s_nop 0
	v_cvt_pk_bf16_f32 v36, v40, v41
	v_cvt_pk_bf16_f32 v37, v44, v45
	global_store_dwordx4 v[38:39], v[34:37], off offset:256
	s_waitcnt vmcnt(15)
	v_lshlrev_b32_e32 v38, 16, v130
	v_and_b32_e32 v39, 0xffff0000, v130
	v_lshlrev_b32_e32 v34, 16, v128
	v_and_b32_e32 v35, 0xffff0000, v128
	v_lshlrev_b32_e32 v40, 16, v131
	v_and_b32_e32 v41, 0xffff0000, v131
	v_pk_add_f32 v[22:23], v[22:23], v[34:35]
	v_lshlrev_b32_e32 v36, 16, v129
	v_and_b32_e32 v37, 0xffff0000, v129
	v_pk_add_f32 v[34:35], v[20:21], v[40:41]
	v_pk_add_f32 v[20:21], v[18:19], v[38:39]
	v_cvt_pk_bf16_f32 v18, v22, v23
	v_lshl_add_u64 v[22:23], s[20:21], 0, v[136:137]
	v_pk_add_f32 v[24:25], v[24:25], v[36:37]
	v_lshl_add_u64 v[22:23], v[22:23], 0, v[154:155]
	v_cvt_pk_bf16_f32 v19, v24, v25
	v_cvt_pk_bf16_f32 v20, v20, v21
	v_cvt_pk_bf16_f32 v21, v34, v35
	global_store_dwordx4 v[22:23], v[18:21], off
	s_waitcnt vmcnt(15)
	v_lshlrev_b32_e32 v24, 16, v134
	v_and_b32_e32 v25, 0xffff0000, v134
	v_lshlrev_b32_e32 v18, 16, v132
	v_and_b32_e32 v19, 0xffff0000, v132
	v_lshlrev_b32_e32 v20, 16, v133
	v_and_b32_e32 v21, 0xffff0000, v133
	v_pk_add_f32 v[18:19], v[30:31], v[18:19]
	v_lshlrev_b32_e32 v34, 16, v135
	v_and_b32_e32 v35, 0xffff0000, v135
	v_pk_add_f32 v[20:21], v[32:33], v[20:21]
	v_cvt_pk_bf16_f32 v18, v18, v19
	v_pk_add_f32 v[28:29], v[28:29], v[34:35]
	v_cvt_pk_bf16_f32 v19, v20, v21
	v_pk_add_f32 v[24:25], v[26:27], v[24:25]
	s_nop 0
	v_cvt_pk_bf16_f32 v20, v24, v25
	v_cvt_pk_bf16_f32 v21, v28, v29
	global_store_dwordx4 v[22:23], v[18:21], off offset:256
	s_waitcnt vmcnt(15)
	v_lshlrev_b32_e32 v22, 16, v72
	v_and_b32_e32 v23, 0xffff0000, v72
	v_lshlrev_b32_e32 v18, 16, v70
	v_and_b32_e32 v19, 0xffff0000, v70
	v_lshlrev_b32_e32 v24, 16, v73
	v_and_b32_e32 v25, 0xffff0000, v73
	v_pk_add_f32 v[6:7], v[6:7], v[18:19]
	v_lshlrev_b32_e32 v20, 16, v71
	v_and_b32_e32 v21, 0xffff0000, v71
	v_pk_add_f32 v[18:19], v[4:5], v[24:25]
	v_pk_add_f32 v[4:5], v[2:3], v[22:23]
	v_cvt_pk_bf16_f32 v2, v6, v7
	v_lshl_add_u64 v[6:7], s[20:21], 0, v[74:75]
	v_pk_add_f32 v[8:9], v[8:9], v[20:21]
	v_lshl_add_u64 v[6:7], v[6:7], 0, v[154:155]
	v_cvt_pk_bf16_f32 v3, v8, v9
	v_cvt_pk_bf16_f32 v4, v4, v5
	v_cvt_pk_bf16_f32 v5, v18, v19
	global_store_dwordx4 v[6:7], v[2:5], off
	s_waitcnt vmcnt(15)
	v_lshlrev_b32_e32 v8, 16, v68
	v_and_b32_e32 v9, 0xffff0000, v68
	v_lshlrev_b32_e32 v2, 16, v66
	v_and_b32_e32 v3, 0xffff0000, v66
	v_lshlrev_b32_e32 v4, 16, v67
	v_and_b32_e32 v5, 0xffff0000, v67
	v_lshlrev_b32_e32 v18, 16, v69
	v_and_b32_e32 v19, 0xffff0000, v69
	v_pk_add_f32 v[4:5], v[16:17], v[4:5]
	v_pk_add_f32 v[2:3], v[14:15], v[2:3]
	v_pk_add_f32 v[12:13], v[12:13], v[18:19]
	v_pk_add_f32 v[8:9], v[10:11], v[8:9]
	v_cvt_pk_bf16_f32 v2, v2, v3
	v_cvt_pk_bf16_f32 v3, v4, v5
	s_nop 0
	v_cvt_pk_bf16_f32 v4, v8, v9
	v_cvt_pk_bf16_f32 v5, v12, v13
	global_store_dwordx4 v[6:7], v[2:5], off offset:256
	s_cbranch_vccnz .LBB0_1190
	s_andn2_b64 vcc, exec, s[16:17]
	s_cbranch_vccnz .LBB0_1189
	s_barrier
	s_branch .LBB0_1189

; __global__ void __launch_bounds__(NWAVES * 64, 2) mega_fwd(Args args) {
	.amdhsa_kernel _Z8mega_fwd4Args
		.amdhsa_group_segment_fixed_size 0
		.amdhsa_private_segment_fixed_size 0
		.amdhsa_kernarg_size 432
		.amdhsa_user_sgpr_count 2
		.amdhsa_user_sgpr_dispatch_ptr 0
		.amdhsa_user_sgpr_queue_ptr 0
		.amdhsa_user_sgpr_kernarg_segment_ptr 1
		.amdhsa_user_sgpr_dispatch_id 0
		.amdhsa_user_sgpr_kernarg_preload_length 0
		.amdhsa_user_sgpr_kernarg_preload_offset 0
		.amdhsa_user_sgpr_private_segment_size 0
		.amdhsa_uses_dynamic_stack 0
		.amdhsa_enable_private_segment 0
		.amdhsa_system_sgpr_workgroup_id_x 1
		.amdhsa_system_sgpr_workgroup_id_y 0
		.amdhsa_system_sgpr_workgroup_id_z 0
		.amdhsa_system_sgpr_workgroup_info 0
		.amdhsa_system_vgpr_workitem_id 0
		.amdhsa_next_free_vgpr 256
		.amdhsa_next_free_sgpr 102
		.amdhsa_accum_offset 256
		.amdhsa_reserve_vcc 1
		.amdhsa_float_round_mode_32 0
		.amdhsa_float_round_mode_16_64 0
		.amdhsa_float_denorm_mode_32 3
		.amdhsa_float_denorm_mode_16_64 3
		.amdhsa_dx10_clamp 1
		.amdhsa_ieee_mode 1
		.amdhsa_fp16_overflow 0
		.amdhsa_tg_split 0
		.amdhsa_exception_fp_ieee_invalid_op 0
		.amdhsa_exception_fp_denorm_src 0
		.amdhsa_exception_fp_ieee_div_zero 0
		.amdhsa_exception_fp_ieee_overflow 0
		.amdhsa_exception_fp_ieee_underflow 0
		.amdhsa_exception_fp_ieee_inexact 0
		.amdhsa_exception_int_div_zero 0
	.end_amdhsa_kernel

; __global__ void __launch_bounds__(NWAVES * 64, 2) mega_fwd(Args args) {
.Lfunc_end0:
	.size	_Z8mega_fwd4Args, .Lfunc_end0-_Z8mega_fwd4Args
	.set _Z8mega_fwd4Args.num_vgpr, 256
	.set _Z8mega_fwd4Args.num_agpr, 0
	.set _Z8mega_fwd4Args.numbered_sgpr, 102
	.set _Z8mega_fwd4Args.num_named_barrier, 0
	.set _Z8mega_fwd4Args.private_seg_size, 0
	.set _Z8mega_fwd4Args.uses_vcc, 1
	.set _Z8mega_fwd4Args.uses_flat_scratch, 0
	.set _Z8mega_fwd4Args.has_dyn_sized_stack, 0
	.set _Z8mega_fwd4Args.has_recursion, 0
	.set _Z8mega_fwd4Args.has_indirect_call, 0

; __global__ void __launch_bounds__(NWAVES * 64, 2) mega_fwd(Args args) {
amdhsa.kernels:
  - .agpr_count:     0
    .args:
      - .offset:         0
        .size:           176
        .value_kind:     by_value
      - .offset:         176
        .size:           4
        .value_kind:     hidden_block_count_x
      - .offset:         180
        .size:           4
        .value_kind:     hidden_block_count_y
      - .offset:         184
        .size:           4
        .value_kind:     hidden_block_count_z
      - .offset:         188
        .size:           2
        .value_kind:     hidden_group_size_x
      - .offset:         190
        .size:           2
        .value_kind:     hidden_group_size_y
      - .offset:         192
        .size:           2
        .value_kind:     hidden_group_size_z
      - .offset:         194
        .size:           2
        .value_kind:     hidden_remainder_x
      - .offset:         196
        .size:           2
        .value_kind:     hidden_remainder_y
      - .offset:         198
        .size:           2
        .value_kind:     hidden_remainder_z
      - .offset:         216
        .size:           8
        .value_kind:     hidden_global_offset_x
      - .offset:         224
        .size:           8
        .value_kind:     hidden_global_offset_y
      - .offset:         232
        .size:           8
        .value_kind:     hidden_global_offset_z
      - .offset:         240
        .size:           2
        .value_kind:     hidden_grid_dims
      - .offset:         296
        .size:           4
        .value_kind:     hidden_dynamic_lds_size
    .group_segment_fixed_size: 0
    .kernarg_segment_align: 8
    .kernarg_segment_size: 432
    .language:       OpenCL C
    .language_version:
      - 2
      - 0
    .max_flat_workgroup_size: 512
    .name:           _Z8mega_fwd4Args
    .private_segment_fixed_size: 0
    .sgpr_count:     108
    .sgpr_spill_count: 0
    .symbol:         _Z8mega_fwd4Args.kd
    .uniform_work_group_size: 1
    .uses_dynamic_stack: false
    .vgpr_count:     256
    .vgpr_spill_count: 0
    .wavefront_size: 64
